# baseline (speedup 1.0000x reference)
.Lp4_last:
	s_lshl_b32 s48, s17, 18
	s_or_b32 s49, s49, s48
	s_mov_b32 m0, s28
	s_lshl_b32 s49, s49, 1
	ds_read_b128 v[162:165], v226 offset:49152
	ds_read_b128 v[166:169], v226 offset:51200
	ds_read_b128 v[170:173], v227 offset:49152
	ds_read_b128 v[174:177], v227 offset:51200
	ds_read_b128 v[178:181], v226 offset:53248
	ds_read_b128 v[182:185], v226 offset:55296
	ds_read_b128 v[186:189], v227 offset:53248
	ds_read_b128 v[190:193], v227 offset:55296
	buffer_load_dwordx4 v199, s[8:11], s49 offen lds
	s_mov_b32 m0, s29
	s_or_b32 s48, s51, s48
	buffer_load_dwordx4 v205, s[8:11], s49 offen lds
	s_lshl_b32 s48, s48, 1
	s_mov_b32 m0, s30
	s_lshl_b32 s17, s17, 22
	buffer_load_dwordx4 v199, s[8:11], s48 offen lds
	s_mov_b32 m0, s31
	s_add_i32 s17, s17, s47
	buffer_load_dwordx4 v205, s[8:11], s48 offen lds
	s_mov_b32 m0, s33
	s_nop 0
	buffer_load_dwordx4 v1, s[4:7], s17 offen lds
	s_mov_b32 m0, s34
	s_nop 0
	buffer_load_dwordx4 v204, s[4:7], s17 offen lds
	v_exp_f32_e32 v244, v114
	v_exp_f32_e32 v245, v115
	v_exp_f32_e32 v246, v116
	v_exp_f32_e32 v247, v117
	v_exp_f32_e32 v248, v78
	v_exp_f32_e32 v249, v79
	v_exp_f32_e32 v250, v80
	v_exp_f32_e32 v251, v81
	v_exp_f32_e32 v252, v106
	v_exp_f32_e32 v253, v107
	v_exp_f32_e32 v254, v108
	v_exp_f32_e32 v255, v109
	v_exp_f32_e32 v232, v70
	v_exp_f32_e32 v233, v71
	v_exp_f32_e32 v234, v72
	v_exp_f32_e32 v235, v73
	s_waitcnt lgkmcnt(0)
	s_waitcnt vmcnt(8)
	s_barrier
	s_setprio 1
	s_waitcnt lgkmcnt(0)
	v_mfma_f32_16x16x32_bf16 v[90:93], v[162:165], v[130:133], v[90:93]
	v_mfma_f32_16x16x32_bf16 v[86:89], v[162:165], v[138:141], v[86:89]
	v_mfma_f32_16x16x32_bf16 v[42:45], v[166:169], v[130:133], v[42:45]
	v_mfma_f32_16x16x32_bf16 v[38:41], v[166:169], v[138:141], v[38:41]
	v_mfma_f32_16x16x32_bf16 v[126:129], v[178:181], v[130:133], v[126:129]
	v_mfma_f32_16x16x32_bf16 v[122:125], v[178:181], v[138:141], v[122:125]
	v_mfma_f32_16x16x32_bf16 v[58:61], v[182:185], v[130:133], v[58:61]
	v_mfma_f32_16x16x32_bf16 v[50:53], v[182:185], v[138:141], v[50:53]
	v_mfma_f32_16x16x32_bf16 v[90:93], v[170:173], v[134:137], v[90:93]
	v_mfma_f32_16x16x32_bf16 v[86:89], v[170:173], v[142:145], v[86:89]
	v_mfma_f32_16x16x32_bf16 v[42:45], v[174:177], v[134:137], v[42:45]
	v_mfma_f32_16x16x32_bf16 v[38:41], v[174:177], v[142:145], v[38:41]
	v_mfma_f32_16x16x32_bf16 v[126:129], v[186:189], v[134:137], v[126:129]
	v_mfma_f32_16x16x32_bf16 v[122:125], v[186:189], v[142:145], v[122:125]
	v_mfma_f32_16x16x32_bf16 v[58:61], v[190:193], v[134:137], v[58:61]
	v_mfma_f32_16x16x32_bf16 v[50:53], v[190:193], v[142:145], v[50:53]
	s_setprio 0
	s_setprio 1
	v_mfma_f32_16x16x32_bf16 v[82:85], v[162:165], v[146:149], v[82:85]
	v_mfma_f32_16x16x32_bf16 v[22:25], v[162:165], v[154:157], v[22:25]
	v_mfma_f32_16x16x32_bf16 v[34:37], v[166:169], v[146:149], v[34:37]
	v_mfma_f32_16x16x32_bf16 v[6:9], v[166:169], v[154:157], v[6:9]
	v_mfma_f32_16x16x32_bf16 v[118:121], v[178:181], v[146:149], v[118:121]
	v_mfma_f32_16x16x32_bf16 v[30:33], v[178:181], v[154:157], v[30:33]
	v_mfma_f32_16x16x32_bf16 v[46:49], v[182:185], v[146:149], v[46:49]
	v_mfma_f32_16x16x32_bf16 v[14:17], v[182:185], v[154:157], v[14:17]
	v_mfma_f32_16x16x32_bf16 v[82:85], v[170:173], v[150:153], v[82:85]
	v_mfma_f32_16x16x32_bf16 v[22:25], v[170:173], v[158:161], v[22:25]
	v_mfma_f32_16x16x32_bf16 v[34:37], v[174:177], v[150:153], v[34:37]
	v_mfma_f32_16x16x32_bf16 v[6:9], v[174:177], v[158:161], v[6:9]
	v_mfma_f32_16x16x32_bf16 v[118:121], v[186:189], v[150:153], v[118:121]
	v_mfma_f32_16x16x32_bf16 v[30:33], v[186:189], v[158:161], v[30:33]
	v_mfma_f32_16x16x32_bf16 v[46:49], v[190:193], v[150:153], v[46:49]
	v_mfma_f32_16x16x32_bf16 v[14:17], v[190:193], v[158:161], v[14:17]
	s_setprio 0
	s_barrier
